# v25 + top-k: all four score-row load groups issued before one wait
# baseline (speedup 1.0000x reference)
.LBB0_511:
	v_writelane_b32 v254, s2, 34
	s_ashr_i32 s1, s0, 31
	s_bfe_u32 s33, s0, 0x60006
	s_lshl_b64 s[2:3], s[0:1], 9
	v_readlane_b32 s5, v254, 30
	s_add_u32 s6, s5, s2
	v_readlane_b32 s2, v254, 31
	s_addc_u32 s7, s2, s3
	v_writelane_b32 v254, s6, 35
	s_cmp_gt_u32 s33, 3
	s_mov_b64 s[2:3], -1
	v_writelane_b32 v254, s7, 36
	s_cbranch_scc0 .LBB0_1171
	s_lshl_b64 s[0:1], s[0:1], 13
	v_readlane_b32 s2, v254, 28
	s_add_u32 s6, s2, s0
	v_readlane_b32 s0, v254, 29
	s_addc_u32 s7, s0, s1
	v_lshlrev_b32_e32 v32, 1, v0
	global_load_ushort v105, v32, s[6:7]
	global_load_ushort v128, v32, s[6:7] offset:128
	global_load_ushort v129, v32, s[6:7] offset:256
	global_load_ushort v143, v32, s[6:7] offset:384
	global_load_ushort v144, v32, s[6:7] offset:512
	global_load_ushort v145, v32, s[6:7] offset:640
	global_load_ushort v146, v32, s[6:7] offset:768
	global_load_ushort v147, v32, s[6:7] offset:896
	global_load_ushort v148, v32, s[6:7] offset:1024
	global_load_ushort v149, v32, s[6:7] offset:1152
	global_load_ushort v159, v32, s[6:7] offset:1280
	global_load_ushort v160, v32, s[6:7] offset:1408
	global_load_ushort v161, v32, s[6:7] offset:1536
	global_load_ushort v162, v32, s[6:7] offset:1664
	global_load_ushort v163, v32, s[6:7] offset:1792
	global_load_ushort v164, v32, s[6:7] offset:1920
	v_lshl_add_u64 v[74:75], s[6:7], 0, v[32:33]
	v_mov_b32_e32 v104, 0
	v_mov_b32_e32 v124, 0
	v_mov_b32_e32 v122, 0
	v_mov_b32_e32 v130, 0
	v_mov_b32_e32 v126, 0
	v_mov_b32_e32 v132, 0
	v_mov_b32_e32 v131, 0
	v_mov_b32_e32 v134, 0
	v_mov_b32_e32 v133, 0
	v_mov_b32_e32 v136, 0
	v_mov_b32_e32 v135, 0
	v_mov_b32_e32 v138, 0
	v_mov_b32_e32 v137, 0
	v_mov_b32_e32 v140, 0
	v_mov_b32_e32 v139, 0
	v_mov_b32_e32 v142, 0
	v_mov_b32_e32 v141, 0
	v_mov_b32_e32 v108, 0
	v_mov_b32_e32 v112, 0
	v_mov_b32_e32 v111, 0
	v_mov_b32_e32 v114, 0
	v_mov_b32_e32 v113, 0
	v_mov_b32_e32 v116, 0
	v_mov_b32_e32 v115, 0
	v_mov_b32_e32 v118, 0
	v_mov_b32_e32 v117, 0
	v_mov_b32_e32 v120, 0
	v_mov_b32_e32 v119, 0
	v_mov_b32_e32 v123, 0
	v_mov_b32_e32 v121, 0
	v_mov_b32_e32 v127, 0
	v_mov_b32_e32 v125, 0
	v_mov_b32_e32 v3, 0
	v_mov_b32_e32 v5, 0
	v_mov_b32_e32 v95, 0
	v_mov_b32_e32 v94, 0
	v_mov_b32_e32 v97, 0
	v_mov_b32_e32 v96, 0
	v_mov_b32_e32 v99, 0
	v_mov_b32_e32 v98, 0
	v_mov_b32_e32 v101, 0
	v_mov_b32_e32 v100, 0
	v_mov_b32_e32 v103, 0
	v_mov_b32_e32 v102, 0
	v_mov_b32_e32 v107, 0
	v_mov_b32_e32 v106, 0
	v_mov_b32_e32 v110, 0
	v_mov_b32_e32 v109, 0
	s_waitcnt lgkmcnt(0)
	s_cmp_lt_u32 s33, 16
	s_cselect_b64 s[0:1], -1, 0
	s_cbranch_scc1 .Ltk_g1_done
	global_load_ushort v142, v[74:75], off offset:2048
	global_load_ushort v141, v[74:75], off offset:2176
	global_load_ushort v140, v[74:75], off offset:2304
	global_load_ushort v139, v[74:75], off offset:2432
	global_load_ushort v138, v[74:75], off offset:2560
	global_load_ushort v137, v[74:75], off offset:2688
	global_load_ushort v136, v[74:75], off offset:2816
	global_load_ushort v135, v[74:75], off offset:2944
	global_load_ushort v134, v[74:75], off offset:3072
	global_load_ushort v133, v[74:75], off offset:3200
	global_load_ushort v132, v[74:75], off offset:3328
	global_load_ushort v131, v[74:75], off offset:3456
	global_load_ushort v130, v[74:75], off offset:3584
	global_load_ushort v126, v[74:75], off offset:3712
	global_load_ushort v124, v[74:75], off offset:3840
	global_load_ushort v122, v[74:75], off offset:3968
.Ltk_g1_done:
	v_mov_b32_e32 v32, 0
	s_cmp_lt_u32 s33, 32
	s_cselect_b64 s[2:3], -1, 0
	s_cbranch_scc1 .Ltk_g2_done
	v_lshlrev_b32_e32 v221, 1, v4
	v_lshlrev_b32_e32 v222, 1, v6
	v_lshlrev_b32_e32 v223, 1, v8
	v_lshlrev_b32_e32 v224, 1, v10
	global_load_ushort v127, v221, s[6:7]
	global_load_ushort v125, v222, s[6:7]
	global_load_ushort v123, v223, s[6:7]
	global_load_ushort v121, v224, s[6:7]
	v_lshlrev_b32_e32 v221, 1, v12
	v_lshlrev_b32_e32 v222, 1, v14
	v_lshlrev_b32_e32 v223, 1, v16
	v_lshlrev_b32_e32 v224, 1, v18
	global_load_ushort v120, v221, s[6:7]
	global_load_ushort v119, v222, s[6:7]
	global_load_ushort v118, v223, s[6:7]
	global_load_ushort v117, v224, s[6:7]
	v_lshlrev_b32_e32 v221, 1, v20
	v_lshlrev_b32_e32 v222, 1, v22
	v_lshlrev_b32_e32 v223, 1, v24
	v_lshlrev_b32_e32 v224, 1, v26
	global_load_ushort v116, v221, s[6:7]
	global_load_ushort v115, v222, s[6:7]
	global_load_ushort v114, v223, s[6:7]
	global_load_ushort v113, v224, s[6:7]
	v_lshlrev_b32_e32 v221, 1, v28
	v_lshlrev_b32_e32 v222, 1, v30
	v_lshlrev_b32_e32 v223, 1, v38
	v_lshlrev_b32_e32 v224, 1, v40
	global_load_ushort v112, v221, s[6:7]
	global_load_ushort v111, v222, s[6:7]
	global_load_ushort v104, v223, s[6:7]
	global_load_ushort v108, v224, s[6:7]
.Ltk_g2_done:
	s_cmp_lt_u32 s33, 48
	s_cselect_b64 s[4:5], -1, 0
	s_and_b64 vcc, exec, s[4:5]
	s_cbranch_vccnz .Ltk_g3_done
	v_lshlrev_b32_e32 v221, 1, v42
	v_lshlrev_b32_e32 v222, 1, v44
	v_lshlrev_b32_e32 v223, 1, v46
	v_lshlrev_b32_e32 v224, 1, v48
	global_load_ushort v110, v221, s[6:7]
	global_load_ushort v109, v222, s[6:7]
	global_load_ushort v107, v223, s[6:7]
	global_load_ushort v106, v224, s[6:7]
	v_lshlrev_b32_e32 v221, 1, v50
	v_lshlrev_b32_e32 v222, 1, v52
	v_lshlrev_b32_e32 v223, 1, v54
	v_lshlrev_b32_e32 v224, 1, v56
	global_load_ushort v103, v221, s[6:7]
	global_load_ushort v102, v222, s[6:7]
	global_load_ushort v101, v223, s[6:7]
	global_load_ushort v100, v224, s[6:7]
	v_lshlrev_b32_e32 v221, 1, v58
	v_lshlrev_b32_e32 v222, 1, v60
	v_lshlrev_b32_e32 v223, 1, v62
	v_lshlrev_b32_e32 v224, 1, v64
	global_load_ushort v99, v221, s[6:7]
	global_load_ushort v98, v222, s[6:7]
	global_load_ushort v97, v223, s[6:7]
	global_load_ushort v96, v224, s[6:7]
	v_lshlrev_b32_e32 v221, 1, v66
	v_lshlrev_b32_e32 v222, 1, v68
	v_lshlrev_b32_e32 v223, 1, v70
	v_lshlrev_b32_e32 v224, 1, v72
	global_load_ushort v95, v221, s[6:7]
	global_load_ushort v94, v222, s[6:7]
	global_load_ushort v32, v223, s[6:7]
	global_load_ushort v5, v224, s[6:7]
.Ltk_g3_done:
	s_waitcnt vmcnt(0)
	v_cvt_f32_f16_e32 v142, v142
	v_cvt_f32_f16_e32 v141, v141
	v_cvt_f32_f16_e32 v140, v140
	v_cvt_f32_f16_e32 v139, v139
	v_cvt_f32_f16_e32 v138, v138
	v_cvt_f32_f16_e32 v137, v137
	v_cvt_f32_f16_e32 v136, v136
	v_cvt_f32_f16_e32 v135, v135
	v_cvt_f32_f16_e32 v134, v134
	v_cvt_f32_f16_e32 v133, v133
	v_cvt_f32_f16_e32 v132, v132
	v_cvt_f32_f16_e32 v131, v131
	v_cvt_f32_f16_e32 v130, v130
	v_cvt_f32_f16_e32 v126, v126
	v_cvt_f32_f16_e32 v124, v124
	v_cvt_f32_f16_e32 v122, v122
	v_cvt_f32_f16_e32 v127, v127
	v_cvt_f32_f16_e32 v125, v125
	v_cvt_f32_f16_e32 v123, v123
	v_cvt_f32_f16_e32 v121, v121
	v_cvt_f32_f16_e32 v120, v120
	v_cvt_f32_f16_e32 v119, v119
	v_cvt_f32_f16_e32 v118, v118
	v_cvt_f32_f16_e32 v117, v117
	v_cvt_f32_f16_e32 v116, v116
	v_cvt_f32_f16_e32 v115, v115
	v_cvt_f32_f16_e32 v114, v114
	v_cvt_f32_f16_e32 v113, v113
	v_cvt_f32_f16_e32 v112, v112
	v_cvt_f32_f16_e32 v111, v111
	v_cvt_f32_f16_e32 v104, v104
	v_cvt_f32_f16_e32 v108, v108
	v_cvt_f32_f16_e32 v110, v110
	v_cvt_f32_f16_e32 v109, v109
	v_cvt_f32_f16_e32 v107, v107
	v_cvt_f32_f16_e32 v106, v106
	v_cvt_f32_f16_e32 v103, v103
	v_cvt_f32_f16_e32 v102, v102
	v_cvt_f32_f16_e32 v101, v101
	v_cvt_f32_f16_e32 v100, v100
	v_cvt_f32_f16_e32 v99, v99
	v_cvt_f32_f16_e32 v98, v98
	v_cvt_f32_f16_e32 v97, v97
	v_cvt_f32_f16_e32 v96, v96
	v_cvt_f32_f16_e32 v95, v95
	v_cvt_f32_f16_e32 v94, v94
	v_cvt_f32_f16_e32 v32, v32
	v_cvt_f32_f16_e32 v5, v5
